# baseline (speedup 1.0000x reference)
.LBB1_48:
	s_or_b64 exec, exec, s[0:1]
	s_add_i32 s27, s30, 1
	s_lshl_b32 s0, s27, 18
	s_add_u32 s4, s44, s0
	s_addc_u32 s5, s45, 0
	s_lshl_b32 s0, s30, 2
	v_readlane_b32 s1, v240, 2
	s_add_i32 s0, s0, s1
	s_lshl_b32 s8, s0, 2
	s_mov_b32 s9, s31
	s_lshl_b64 s[0:1], s[8:9], 8
	s_add_u32 s0, s62, s0
	s_addc_u32 s1, s63, s1
	v_cmp_gt_i32_e32 vcc, 64, v179
	s_waitcnt lgkmcnt(0)
	s_barrier
	s_and_saveexec_b64 s[20:21], vcc
	s_cbranch_execz .LBB1_52
	v_ashrrev_i32_e32 v98, 5, v179
	v_bfe_u32 v101, v179, 1, 4
	v_and_b32_e32 v103, 1, v179
	s_add_i32 s9, 0, 0x18000
	v_lshl_add_u32 v104, v98, 9, s9
	v_lshlrev_b32_e32 v105, 5, v101
	v_lshlrev_b32_e32 v106, 4, v103
	v_add3_u32 v106, v104, v105, v106
	v_lshlrev_b32_e32 v110, 13, v98
	ds_read_b128 v[104:107], v106
	v_ashrrev_i32_e32 v111, 31, v110
	v_or_b32_e32 v103, s74, v103
	v_lshl_add_u64 v[110:111], v[110:111], 4, s[4:5]
	v_lshl_add_u64 v[110:111], s[28:29], 4, v[110:111]
	v_lshlrev_b32_e32 v98, 8, v103
	v_lshl_add_u64 v[110:111], v[110:111], 0, v[98:99]
	v_lshlrev_b32_e32 v98, 4, v101
	v_lshl_add_u64 v[110:111], v[110:111], 0, v[98:99]
	s_waitcnt lgkmcnt(0)
	global_store_dwordx4 v[110:111], v[104:107], off sc0 sc1
	s_waitcnt vmcnt(0)
	v_cmp_eq_u32_e32 vcc, 0, v179
	s_and_b64 exec, exec, vcc
	s_cbranch_execz .LBB1_52
	s_mov_b64 s[96:97], exec
	v_mbcnt_lo_u32_b32 v98, s96, 0
	v_mbcnt_hi_u32_b32 v98, s97, v98
	v_cmp_eq_u32_e32 vcc, 0, v98
	s_and_b64 vcc, exec, vcc
	s_mov_b64 exec, vcc
	s_cbranch_execz .LBB1_52
	v_readlane_b32 s9, v240, 14
	s_lshl_b32 s9, s9, 2
	s_bcnt1_i32_b64 s91, s[96:97]
	v_mov_b32_e32 v98, s9
	v_mov_b32_e32 v101, s91
	global_atomic_add v98, v101, s[0:1]

.LBB1_69:
	s_or_b64 exec, exec, s[4:5]
	s_add_i32 s0, s8, 0x200
	s_mov_b32 s1, s31
	s_lshl_b32 s9, s27, 17
	s_lshl_b64 s[0:1], s[0:1], 8
	s_add_u32 s4, s62, s0
	s_addc_u32 s5, s63, s1
	s_lshl_b32 s9, s9, 1
	s_add_u32 s0, s46, s9
	s_addc_u32 s1, s47, 0
	v_cmp_gt_i32_e32 vcc, 64, v179
	s_waitcnt lgkmcnt(0)
	s_barrier
	s_and_saveexec_b64 s[18:19], vcc
	s_cbranch_execz .LBB1_73
	v_ashrrev_i32_e32 v98, 5, v179
	v_bfe_u32 v103, v179, 1, 4
	v_and_b32_e32 v100, 1, v179
	s_add_i32 s20, 0, 0x18000
	v_lshl_add_u32 v101, v98, 9, s20
	v_lshlrev_b32_e32 v104, 5, v103
	v_lshlrev_b32_e32 v105, 4, v100
	v_add3_u32 v104, v101, v104, v105
	v_or_b32_e32 v105, s74, v100
	v_lshlrev_b32_e32 v100, 13, v98
	v_lshlrev_b32_e32 v98, 8, v105
	ds_read_b128 v[104:107], v104
	v_ashrrev_i32_e32 v101, 31, v100
	v_lshl_add_u64 v[100:101], v[100:101], 4, s[0:1]
	v_lshl_add_u64 v[100:101], s[28:29], 4, v[100:101]
	v_lshl_add_u64 v[100:101], v[100:101], 0, v[98:99]
	v_lshlrev_b32_e32 v98, 4, v103
	v_lshl_add_u64 v[100:101], v[100:101], 0, v[98:99]
	s_waitcnt lgkmcnt(0)
	global_store_dwordx4 v[100:101], v[104:107], off sc0 sc1
	s_waitcnt vmcnt(0)
	v_cmp_eq_u32_e32 vcc, 0, v179
	s_and_b64 exec, exec, vcc
	s_cbranch_execz .LBB1_73
	s_mov_b64 s[20:21], exec
	v_mbcnt_lo_u32_b32 v98, s20, 0
	v_mbcnt_hi_u32_b32 v98, s21, v98
	v_cmp_eq_u32_e32 vcc, 0, v98
	s_and_b64 s[96:97], exec, vcc
	s_mov_b64 exec, s[96:97]
	s_cbranch_execz .LBB1_73
	v_readlane_b32 s91, v240, 14
	s_lshl_b32 s91, s91, 2
	s_bcnt1_i32_b64 s20, s[20:21]
	v_mov_b32_e32 v98, s91
	v_mov_b32_e32 v100, s20
	global_atomic_add v98, v100, s[4:5]
